# speedup vs baseline: 1.0816x; 1.0816x over previous
.LBB1_30:
	s_or_b64 exec, exec, s[0:1]
	s_waitcnt lgkmcnt(0)
	s_barrier
	ds_read_b64 v[2:3], v109
	s_mov_b64 s[0:1], -1
	s_waitcnt lgkmcnt(0)
	s_barrier
	v_mov_b32_e32 v234, v2
	v_cmp_lt_i32_e32 vcc, -1, v2
	s_and_saveexec_b64 s[92:93], vcc
	s_cbranch_execz .LBB1_3
	v_and_b32_e32 v4, 0x7fffffe1, v2
	v_cmp_ne_u32_e32 vcc, 1, v4
	s_and_saveexec_b64 s[0:1], vcc
	s_xor_b64 s[0:1], exec, s[0:1]
	v_writelane_b32 v230, s0, 11
	s_nop 1
	v_writelane_b32 v230, s1, 12
	s_cbranch_execz .LBB1_212
	v_cmp_gt_u32_e32 vcc, 32, v2
	s_and_saveexec_b64 s[0:1], vcc
	s_xor_b64 s[0:1], exec, s[0:1]
	v_lshrrev_b32_e32 v4, 3, v2
	v_lshrrev_b32_e32 v2, 1, v2
	s_or_saveexec_b64 s[0:1], s[0:1]
	s_mov_b64 s[2:3], -1
	s_xor_b64 exec, exec, s[0:1]
	s_cbranch_execz .LBB1_44
	v_cmp_lt_u32_e32 vcc, 63, v2
	s_and_saveexec_b64 s[2:3], vcc
	s_xor_b64 s[2:3], exec, s[2:3]
	s_cbranch_execz .LBB1_41
	s_movk_i32 s4, 0x5f
	v_cmp_lt_u32_e32 vcc, s4, v2
	s_and_saveexec_b64 s[4:5], vcc
	s_xor_b64 s[4:5], exec, s[4:5]
	v_add_u32_e32 v4, 0xffffffa0, v2
	v_lshrrev_b32_e32 v4, 2, v4
	v_add_u32_e32 v4, 4, v4
	s_or_saveexec_b64 s[6:7], s[4:5]
	s_mov_b64 s[4:5], 0
	s_xor_b64 exec, exec, s[6:7]
	v_subrev_u32_e32 v4, 64, v2
	v_and_b32_e32 v5, 4, v2
	v_lshrrev_b32_e32 v4, 3, v4
	v_add_u32_e32 v6, 12, v4
	v_cmp_eq_u32_e32 vcc, 0, v5
	s_and_b64 s[4:5], vcc, exec
	s_nop 0
	v_cndmask_b32_e32 v4, v4, v6, vcc
	s_or_b64 exec, exec, s[6:7]

.LBB1_55:
	s_or_b64 exec, exec, s[2:3]
	v_and_b32_e32 v119, 63, v175
	v_lshlrev_b32_e32 v50, 2, v119
	v_add_u32_e32 v51, 0xffffff40, v50
	v_cmp_gt_u32_e32 vcc, 48, v119
	v_or_b32_e32 v111, 0x80, v119
	v_mul_lo_u16_e32 v111, 0xab, v111
	v_cndmask_b32_e32 v54, v51, v50, vcc
	v_or_b32_e32 v50, 64, v119
	v_mul_lo_u16_e32 v50, 43, v50
	v_lshrrev_b16_e32 v181, 11, v50
	v_lshrrev_b16_e32 v186, 13, v111
	v_lshlrev_b16_e32 v50, 4, v181
	v_lshlrev_b16_e32 v111, 4, v186
	v_add_u16_e32 v50, v119, v50
	v_add_u16_e32 v111, v119, v111
	v_ashrrev_i32_e32 v110, 6, v175
	v_lshlrev_b16_e32 v50, 2, v50
	v_lshlrev_b16_e32 v111, 2, v111
	v_cmp_lt_u32_e32 vcc, 47, v119
	v_lshlrev_b32_e32 v108, 2, v118
	v_mov_b32_e32 v55, v109
	v_and_b32_e32 v142, 0xfc, v50
	v_and_b32_e32 v138, 0xfc, v111
	v_lshlrev_b32_e32 v194, 4, v110
	v_cndmask_b32_e64 v192, 0, 1, vcc
	v_lshl_add_u64 v[56:57], s[50:51], 0, v[108:109]
	v_lshlrev_b64 v[116:117], 2, v[54:55]
	v_lshlrev_b32_e32 v114, 2, v142
	v_mov_b32_e32 v115, v109
	v_lshlrev_b32_e32 v112, 2, v138
	v_mov_b32_e32 v113, v109
	v_or_b32_e32 v176, v194, v192
	v_lshl_add_u64 v[52:53], v[56:57], 0, v[116:117]
	v_lshl_add_u64 v[50:51], v[56:57], 0, v[114:115]
	v_lshl_add_u64 v[162:163], v[56:57], 0, v[112:113]
	v_mul_lo_u32 v56, v176, s67
	v_lshlrev_b32_e32 v57, 2, v54
	s_movk_i32 s2, 0xff
	v_add3_u32 v178, 0, v56, v57
	v_bitop3_b16 v56, v175, s2, v169 bitop3:0xc8
	v_mul_lo_u16_e32 v56, 0xab, v56
	v_lshrrev_b16_e32 v191, 13, v56
	v_mul_lo_u16_e32 v56, 48, v191
	v_sub_u16_e32 v56, v175, v56
	v_lshlrev_b16_e32 v203, 2, v56
	v_or_b32_e32 v56, 0x100, v119
	s_movk_i32 s2, 0x556
	v_mul_u32_u24_sdwa v190, v56, s2 dst_sel:DWORD dst_unused:UNUSED_PAD src0_sel:WORD_0 src1_sel:DWORD
	v_mul_lo_u16_sdwa v57, v190, v170 dst_sel:DWORD dst_unused:UNUSED_PAD src0_sel:WORD_1 src1_sel:DWORD
	v_sub_u16_e32 v56, v56, v57
	v_lshlrev_b16_e32 v202, 2, v56
	v_or_b32_e32 v56, 0x140, v119
	v_mul_u32_u24_sdwa v189, v56, s2 dst_sel:DWORD dst_unused:UNUSED_PAD src0_sel:WORD_0 src1_sel:DWORD
	v_mul_lo_u16_sdwa v57, v189, v170 dst_sel:DWORD dst_unused:UNUSED_PAD src0_sel:WORD_1 src1_sel:DWORD
	v_sub_u16_e32 v56, v56, v57
	v_lshlrev_b16_e32 v201, 2, v56
	v_or_b32_e32 v56, 0x180, v119
	v_mul_u32_u24_sdwa v188, v56, s2 dst_sel:DWORD dst_unused:UNUSED_PAD src0_sel:WORD_0 src1_sel:DWORD
	v_mul_lo_u16_sdwa v57, v188, v170 dst_sel:DWORD dst_unused:UNUSED_PAD src0_sel:WORD_1 src1_sel:DWORD
	v_sub_u16_e32 v56, v56, v57
	v_lshlrev_b16_e32 v200, 2, v56
	v_or_b32_e32 v56, 0x1c0, v119
	v_mul_u32_u24_sdwa v187, v56, s2 dst_sel:DWORD dst_unused:UNUSED_PAD src0_sel:WORD_0 src1_sel:DWORD
	v_mul_lo_u16_sdwa v57, v187, v170 dst_sel:DWORD dst_unused:UNUSED_PAD src0_sel:WORD_1 src1_sel:DWORD
	v_sub_u16_e32 v56, v56, v57
	v_lshlrev_b16_e32 v199, 2, v56
	v_or_b32_e32 v56, 0x200, v119
	v_mul_u32_u24_sdwa v185, v56, s2 dst_sel:DWORD dst_unused:UNUSED_PAD src0_sel:WORD_0 src1_sel:DWORD
	v_mul_lo_u16_sdwa v57, v185, v170 dst_sel:DWORD dst_unused:UNUSED_PAD src0_sel:WORD_1 src1_sel:DWORD
	v_sub_u16_e32 v56, v56, v57
	v_lshlrev_b16_e32 v198, 2, v56
	v_or_b32_e32 v56, 0x240, v119
	v_mul_u32_u24_sdwa v184, v56, s2 dst_sel:DWORD dst_unused:UNUSED_PAD src0_sel:WORD_0 src1_sel:DWORD
	v_mul_lo_u16_sdwa v57, v184, v170 dst_sel:DWORD dst_unused:UNUSED_PAD src0_sel:WORD_1 src1_sel:DWORD
	v_sub_u16_e32 v56, v56, v57
	v_lshlrev_b16_e32 v197, 2, v56
	v_or_b32_e32 v56, 0x280, v119
	v_mul_u32_u24_sdwa v182, v56, s2 dst_sel:DWORD dst_unused:UNUSED_PAD src0_sel:WORD_0 src1_sel:DWORD
	v_mul_lo_u16_sdwa v57, v182, v170 dst_sel:DWORD dst_unused:UNUSED_PAD src0_sel:WORD_1 src1_sel:DWORD
	v_sub_u16_e32 v56, v56, v57
	v_lshl_add_u64 v[110:111], s[46:47], 0, v[108:109]
	v_lshlrev_b16_e32 v196, 2, v56
	v_or_b32_e32 v56, 0x2c0, v119
	v_lshlrev_b32_e32 v108, 1, v118
	v_add_u32_e32 v193, v194, v174
	v_mul_u32_u24_sdwa v183, v56, s2 dst_sel:DWORD dst_unused:UNUSED_PAD src0_sel:WORD_0 src1_sel:DWORD
	v_lshl_add_u64 v[118:119], s[38:39], 0, v[108:109]
	v_or_b32_sdwa v120, v193, v182 dst_sel:DWORD dst_unused:UNUSED_PAD src0_sel:DWORD src1_sel:WORD_1
	v_mul_lo_u16_sdwa v57, v183, v170 dst_sel:DWORD dst_unused:UNUSED_PAD src0_sel:WORD_1 src1_sel:DWORD
	v_mad_i64_i32 v[122:123], s[2:3], v120, s56, v[118:119]
	v_lshlrev_b32_e32 v120, 1, v196
	v_mov_b32_e32 v121, v109
	v_sub_u16_e32 v56, v56, v57
	v_lshl_add_u64 v[128:129], v[122:123], 0, v[120:121]
	v_or_b32_sdwa v122, v193, v184 dst_sel:DWORD dst_unused:UNUSED_PAD src0_sel:DWORD src1_sel:WORD_1
	v_lshlrev_b16_e32 v195, 2, v56
	v_or_b32_sdwa v56, v193, v183 dst_sel:DWORD dst_unused:UNUSED_PAD src0_sel:DWORD src1_sel:WORD_1
	v_mad_i64_i32 v[124:125], s[2:3], v122, s56, v[118:119]
	v_lshlrev_b32_e32 v122, 1, v197
	v_mov_b32_e32 v123, v109
	v_mad_i64_i32 v[56:57], s[2:3], v56, s56, v[118:119]
	v_lshlrev_b32_e32 v108, 1, v195
	v_lshl_add_u64 v[130:131], v[124:125], 0, v[122:123]
	v_or_b32_sdwa v124, v193, v185 dst_sel:DWORD dst_unused:UNUSED_PAD src0_sel:DWORD src1_sel:WORD_1
	v_lshl_add_u64 v[56:57], v[56:57], 0, v[108:109]
	v_mad_i64_i32 v[126:127], s[2:3], v124, s56, v[118:119]
	v_lshlrev_b32_e32 v124, 1, v198
	v_mov_b32_e32 v125, v109
	s_waitcnt vmcnt(0)
	s_barrier
	v_lshl_add_u64 v[132:133], v[126:127], 0, v[124:125]
	global_load_dwordx2 v[126:127], v[56:57], off nt
	global_load_dwordx2 v[136:137], v[128:129], off nt
	global_load_dwordx2 v[146:147], v[130:131], off nt
	global_load_dwordx2 v[148:149], v[132:133], off nt
	v_or_b32_e32 v128, v193, v191
	v_and_b32_e32 v204, 0xfc, v203
	v_mad_i64_i32 v[130:131], s[2:3], v128, s56, v[118:119]
	v_lshlrev_b32_e32 v128, 1, v204
	v_mov_b32_e32 v129, v109
	v_lshl_add_u64 v[134:135], v[130:131], 0, v[128:129]
	v_or_b32_e32 v130, v193, v186
	v_mad_i64_i32 v[132:133], s[2:3], v130, s56, v[118:119]
	v_lshlrev_b32_e32 v130, 1, v138
	v_mov_b32_e32 v131, v109
	v_lshl_add_u64 v[138:139], v[132:133], 0, v[130:131]
	v_or_b32_e32 v132, v193, v181
	v_mad_i64_i32 v[140:141], s[2:3], v132, s56, v[118:119]
	v_lshlrev_b32_e32 v132, 1, v142
	v_mov_b32_e32 v133, v109
	v_or_b32_e32 v142, v193, v192
	v_lshl_add_u64 v[140:141], v[140:141], 0, v[132:133]
	v_mad_i64_i32 v[144:145], s[2:3], v142, s56, v[118:119]
	v_lshlrev_b64 v[142:143], 1, v[54:55]
	v_or_b32_sdwa v56, v193, v187 dst_sel:DWORD dst_unused:UNUSED_PAD src0_sel:DWORD src1_sel:WORD_1
	v_lshl_add_u64 v[54:55], v[144:145], 0, v[142:143]
	global_load_dwordx2 v[158:159], v[134:135], off nt
	global_load_dwordx2 v[160:161], v[138:139], off nt
	global_load_dwordx2 v[164:165], v[140:141], off nt
	global_load_dwordx2 v[166:167], v[54:55], off nt
	v_or_b32_sdwa v140, v193, v189 dst_sel:DWORD dst_unused:UNUSED_PAD src0_sel:DWORD src1_sel:WORD_1
	v_mad_i64_i32 v[56:57], s[2:3], v56, s56, v[118:119]
	v_lshlrev_b32_e32 v134, 1, v199
	v_mov_b32_e32 v135, v109
	v_mad_i64_i32 v[144:145], s[2:3], v140, s56, v[118:119]
	v_lshlrev_b32_e32 v140, 1, v201
	v_mov_b32_e32 v141, v109
	v_lshl_add_u64 v[54:55], v[56:57], 0, v[134:135]
	v_or_b32_sdwa v56, v193, v188 dst_sel:DWORD dst_unused:UNUSED_PAD src0_sel:DWORD src1_sel:WORD_1
	v_lshl_add_u64 v[154:155], v[144:145], 0, v[140:141]
	v_or_b32_sdwa v144, v193, v190 dst_sel:DWORD dst_unused:UNUSED_PAD src0_sel:DWORD src1_sel:WORD_1
	v_mad_i64_i32 v[56:57], s[2:3], v56, s56, v[118:119]
	v_lshlrev_b32_e32 v138, 1, v200
	v_mov_b32_e32 v139, v109
	v_mad_i64_i32 v[150:151], s[2:3], v144, s56, v[118:119]
	v_lshlrev_b32_e32 v144, 1, v202
	v_mov_b32_e32 v145, v109
	v_lshl_add_u64 v[56:57], v[56:57], 0, v[138:139]
	v_lshl_add_u64 v[156:157], v[150:151], 0, v[144:145]
	global_load_dwordx2 v[150:151], v[54:55], off nt
	global_load_dwordx2 v[152:153], v[56:57], off nt
	s_nop 0
	global_load_dwordx2 v[154:155], v[154:155], off nt
	s_nop 0
	global_load_dwordx2 v[156:157], v[156:157], off nt
	v_and_b32_e32 v205, 16, v175
	v_lshrrev_b32_e32 v207, 2, v175
	global_load_dwordx4 v[54:57], v[52:53], off
	v_or_b32_e32 v206, v179, v177
	v_and_or_b32 v180, v207, 12, v180
	v_bitop3_b32 v177, v179, v205, v177 bitop3:0x36
	global_load_dwordx4 v[50:53], v[50:51], off
	v_lshlrev_b32_e32 v177, 2, v177
	v_mul_lo_u32 v179, v180, s67
	v_add3_u32 v177, 0, v177, v179
	ds_write2st64_b32 v177, v58, v59 offset1:3
	ds_write2st64_b32 v177, v60, v61 offset0:6 offset1:9
	ds_write2st64_b32 v177, v102, v103 offset0:48 offset1:51
	ds_write2st64_b32 v177, v104, v105 offset0:54 offset1:57
	v_add_u32_e32 v58, 16, v206
	v_bitop3_b32 v58, v58, v175, 16 bitop3:0x78
	v_lshlrev_b32_e32 v58, 2, v58
	v_add3_u32 v102, 0, v58, v179
	global_load_dwordx4 v[58:61], v[162:163], off
	ds_write2st64_b32 v102, v78, v79 offset1:3
	v_add_u32_e32 v78, 32, v206
	v_bitop3_b32 v78, v78, v175, 16 bitop3:0x78
	v_lshlrev_b32_e32 v78, 2, v78
	v_add3_u32 v103, 0, v78, v179
	ds_write2st64_b32 v102, v80, v81 offset0:6 offset1:9
	ds_write2st64_b32 v102, v86, v87 offset0:48 offset1:51
	ds_write2st64_b32 v102, v88, v89 offset0:54 offset1:57
	ds_write2st64_b32 v103, v62, v63 offset1:3
	ds_write2st64_b32 v103, v64, v65 offset0:6 offset1:9
	ds_write2st64_b32 v103, v70, v71 offset0:48 offset1:51
	ds_write2st64_b32 v103, v72, v73 offset0:54 offset1:57
	v_add_u32_e32 v62, 0x60, v206
	v_bitop3_b32 v62, v62, v175, 16 bitop3:0x78
	v_lshlrev_b32_e32 v62, 2, v62
	v_add3_u32 v104, 0, v62, v179
	v_add_u32_e32 v62, 0x70, v206
	v_bitop3_b32 v62, v62, v175, 16 bitop3:0x78
	v_lshlrev_b32_e32 v62, 2, v62
	s_movk_i32 s2, 0x80
	ds_write2st64_b32 v104, v94, v95 offset1:3
	ds_write2st64_b32 v104, v96, v97 offset0:6 offset1:9
	ds_write2st64_b32 v104, v98, v99 offset0:48 offset1:51
	ds_write2st64_b32 v104, v100, v101 offset0:54 offset1:57
	v_add3_u32 v101, 0, v62, v179
	v_bitop3_b32 v62, v206, v205, s2 bitop3:0x36
	v_lshlrev_b32_e32 v62, 2, v62
	v_add3_u32 v105, 0, v62, v179
	v_add_u32_e32 v62, v176, v174
	v_mad_i64_i32 v[62:63], s[2:3], v62, s62, v[110:111]
	v_or_b32_e32 v99, v194, v181
	ds_write2st64_b32 v101, v82, v83 offset1:3
	ds_write2st64_b32 v101, v84, v85 offset0:6 offset1:9
	ds_write2st64_b32 v101, v90, v91 offset0:48 offset1:51
	ds_write2st64_b32 v101, v92, v93 offset0:54 offset1:57
	ds_write2st64_b32 v105, v66, v67 offset1:3
	ds_write2st64_b32 v105, v68, v69 offset0:6 offset1:9
	ds_write2st64_b32 v105, v74, v75 offset0:48 offset1:51
	ds_write2st64_b32 v105, v76, v77 offset0:54 offset1:57
	v_lshl_add_u64 v[74:75], v[62:63], 0, v[116:117]
	v_mul_lo_u32 v62, v99, s67
	v_add3_u32 v100, 0, v62, v114
	v_add_u32_e32 v62, v99, v174
	v_mad_i64_i32 v[62:63], s[2:3], v62, s62, v[110:111]
	v_or_b32_e32 v98, v194, v186
	v_lshl_add_u64 v[80:81], v[62:63], 0, v[114:115]
	v_mul_lo_u32 v66, v98, s67
	s_waitcnt lgkmcnt(0)
	s_barrier
	ds_read_b128 v[62:65], v178
	s_waitcnt vmcnt(7)
	v_cvt_f32_f16_e32 v70, v166
	v_cvt_f32_f16_sdwa v71, v166 dst_sel:DWORD dst_unused:UNUSED_PAD src0_sel:WORD_1
	v_cvt_f32_f16_e32 v72, v167
	v_cvt_f32_f16_sdwa v73, v167 dst_sel:DWORD dst_unused:UNUSED_PAD src0_sel:WORD_1
	v_add3_u32 v162, 0, v66, v112
	ds_read_b128 v[66:69], v100
	v_cvt_f32_f16_e32 v76, v164
	v_cvt_f32_f16_sdwa v77, v164 dst_sel:DWORD dst_unused:UNUSED_PAD src0_sel:WORD_1
	v_cvt_f32_f16_e32 v78, v165
	v_cvt_f32_f16_sdwa v79, v165 dst_sel:DWORD dst_unused:UNUSED_PAD src0_sel:WORD_1
	v_cvt_f32_f16_e32 v82, v160
	v_cvt_f32_f16_sdwa v83, v160 dst_sel:DWORD dst_unused:UNUSED_PAD src0_sel:WORD_1
	v_or_b32_e32 v160, v194, v191
	v_cvt_f32_f16_e32 v86, v147
	v_cvt_f32_f16_sdwa v87, v147 dst_sel:DWORD dst_unused:UNUSED_PAD src0_sel:WORD_1
	v_cvt_f32_f16_e32 v88, v126
	v_cvt_f32_f16_e32 v90, v127
	v_cvt_f32_f16_sdwa v91, v127 dst_sel:DWORD dst_unused:UNUSED_PAD src0_sel:WORD_1
	v_cvt_f32_f16_sdwa v89, v126 dst_sel:DWORD dst_unused:UNUSED_PAD src0_sel:WORD_1
	v_add_u32_e32 v163, 0x80, v193
	s_waitcnt vmcnt(6)
	v_cvt_f32_f16_e32 v84, v151
	v_cvt_f32_f16_sdwa v85, v151 dst_sel:DWORD dst_unused:UNUSED_PAD src0_sel:WORD_1
	s_waitcnt vmcnt(2) lgkmcnt(1)
	v_pk_fma_f32 v[64:65], v[72:73], v[56:57], v[64:65]
	v_pk_fma_f32 v[62:63], v[70:71], v[54:55], v[62:63]
	global_store_dwordx4 v[74:75], v[62:65], off nt
	v_cvt_f32_f16_e32 v70, v161
	v_cvt_f32_f16_sdwa v71, v161 dst_sel:DWORD dst_unused:UNUSED_PAD src0_sel:WORD_1
	s_waitcnt vmcnt(2) lgkmcnt(0)
	v_pk_fma_f32 v[64:65], v[78:79], v[52:53], v[68:69]
	v_pk_fma_f32 v[62:63], v[76:77], v[50:51], v[66:67]
	v_xor_b32_e32 v67, 16, v203
	global_store_dwordx4 v[80:81], v[62:65], off nt
	ds_read_b128 v[62:65], v162
	v_and_b32_e32 v67, 0xfc, v67
	v_mul_lo_u32 v66, v160, s67
	v_lshlrev_b32_e32 v67, 2, v67
	v_add3_u32 v161, 0, v66, v67
	ds_read_b128 v[66:69], v161
	v_cvt_f32_f16_e32 v72, v158
	v_cvt_f32_f16_sdwa v73, v158 dst_sel:DWORD dst_unused:UNUSED_PAD src0_sel:WORD_1
	s_waitcnt vmcnt(2) lgkmcnt(1)
	v_pk_fma_f32 v[64:65], v[70:71], v[60:61], v[64:65]
	v_add_u32_e32 v70, v98, v174
	v_mad_i64_i32 v[70:71], s[2:3], v70, s62, v[110:111]
	v_cvt_f32_f16_e32 v74, v159
	v_cvt_f32_f16_sdwa v75, v159 dst_sel:DWORD dst_unused:UNUSED_PAD src0_sel:WORD_1
	v_pk_fma_f32 v[62:63], v[82:83], v[58:59], v[62:63]
	v_lshl_add_u64 v[70:71], v[70:71], 0, v[112:113]
	global_store_dwordx4 v[70:71], v[62:65], off nt
	v_lshlrev_b32_e32 v70, 2, v204
	v_mov_b32_e32 v71, v109
	s_waitcnt lgkmcnt(0)
	v_pk_fma_f32 v[62:63], v[72:73], v[54:55], v[66:67]
	v_add_u32_e32 v66, v160, v174
	v_mad_i64_i32 v[66:67], s[2:3], v66, s62, v[110:111]
	v_pk_fma_f32 v[64:65], v[74:75], v[56:57], v[68:69]
	v_lshl_add_u64 v[66:67], v[66:67], 0, v[70:71]
	global_store_dwordx4 v[66:67], v[62:65], off nt
	v_or_b32_sdwa v158, v194, v190 dst_sel:DWORD dst_unused:UNUSED_PAD src0_sel:DWORD src1_sel:WORD_1
	v_cvt_f32_f16_e32 v66, v156
	v_xor_b32_e32 v63, 16, v202
	v_mul_lo_u32 v62, v158, s67
	v_lshlrev_b32_sdwa v63, v171, v63 dst_sel:DWORD dst_unused:UNUSED_PAD src0_sel:DWORD src1_sel:WORD_0
	v_add3_u32 v159, 0, v62, v63
	ds_read_b128 v[62:65], v159
	v_cvt_f32_f16_sdwa v67, v156 dst_sel:DWORD dst_unused:UNUSED_PAD src0_sel:WORD_1
	v_or_b32_sdwa v156, v194, v189 dst_sel:DWORD dst_unused:UNUSED_PAD src0_sel:DWORD src1_sel:WORD_1
	v_xor_b32_e32 v73, 16, v201
	v_cvt_f32_f16_e32 v68, v157
	v_cvt_f32_f16_sdwa v69, v157 dst_sel:DWORD dst_unused:UNUSED_PAD src0_sel:WORD_1
	v_mul_lo_u32 v72, v156, s67
	v_lshlrev_b32_sdwa v73, v171, v73 dst_sel:DWORD dst_unused:UNUSED_PAD src0_sel:DWORD src1_sel:WORD_0
	v_add3_u32 v157, 0, v72, v73
	ds_read_b128 v[72:75], v157
	s_waitcnt lgkmcnt(1)
	v_pk_fma_f32 v[62:63], v[66:67], v[50:51], v[62:63]
	v_add_u32_e32 v66, v158, v174
	v_cvt_f32_f16_e32 v76, v154
	v_cvt_f32_f16_sdwa v77, v154 dst_sel:DWORD dst_unused:UNUSED_PAD src0_sel:WORD_1
	v_pk_fma_f32 v[64:65], v[68:69], v[52:53], v[64:65]
	v_mad_i64_i32 v[66:67], s[2:3], v66, s62, v[110:111]
	v_lshlrev_b32_e32 v68, 2, v202
	v_mov_b32_e32 v69, v109
	v_cvt_f32_f16_e32 v78, v155
	v_cvt_f32_f16_sdwa v79, v155 dst_sel:DWORD dst_unused:UNUSED_PAD src0_sel:WORD_1
	v_lshl_add_u64 v[66:67], v[66:67], 0, v[68:69]
	global_store_dwordx4 v[66:67], v[62:65], off nt
	v_add_u32_e32 v66, v156, v174
	v_mad_i64_i32 v[66:67], s[2:3], v66, s62, v[110:111]
	s_waitcnt lgkmcnt(0)
	v_pk_fma_f32 v[62:63], v[76:77], v[58:59], v[72:73]
	v_lshlrev_b32_e32 v72, 2, v201
	v_mov_b32_e32 v73, v109
	v_pk_fma_f32 v[64:65], v[78:79], v[60:61], v[74:75]
	v_lshl_add_u64 v[66:67], v[66:67], 0, v[72:73]
	v_or_b32_sdwa v154, v194, v188 dst_sel:DWORD dst_unused:UNUSED_PAD src0_sel:DWORD src1_sel:WORD_1
	global_store_dwordx4 v[66:67], v[62:65], off nt
	v_cvt_f32_f16_e32 v82, v153
	v_cvt_f32_f16_sdwa v83, v153 dst_sel:DWORD dst_unused:UNUSED_PAD src0_sel:WORD_1
	v_mul_lo_u32 v63, v154, s67
	v_lshlrev_b32_e32 v62, 2, v200
	v_add3_u32 v155, 0, v63, v62
	ds_read_b128 v[74:77], v155
	v_cvt_f32_f16_e32 v64, v152
	v_cvt_f32_f16_sdwa v65, v152 dst_sel:DWORD dst_unused:UNUSED_PAD src0_sel:WORD_1
	v_or_b32_sdwa v152, v194, v187 dst_sel:DWORD dst_unused:UNUSED_PAD src0_sel:DWORD src1_sel:WORD_1
	v_mul_lo_u32 v63, v152, s67
	v_lshlrev_b32_e32 v66, 2, v199
	v_add3_u32 v153, 0, v63, v66
	ds_read_b128 v[78:81], v153
	v_add_u32_e32 v63, v154, v174
	s_waitcnt lgkmcnt(1)
	v_pk_fma_f32 v[76:77], v[82:83], v[56:57], v[76:77]
	v_pk_fma_f32 v[74:75], v[64:65], v[54:55], v[74:75]
	v_mad_i64_i32 v[64:65], s[2:3], v63, s62, v[110:111]
	v_mov_b32_e32 v63, v109
	v_cvt_f32_f16_e32 v82, v150
	v_cvt_f32_f16_sdwa v83, v150 dst_sel:DWORD dst_unused:UNUSED_PAD src0_sel:WORD_1
	v_lshl_add_u64 v[64:65], v[64:65], 0, v[62:63]
	global_store_dwordx4 v[64:65], v[74:77], off nt
	v_add_u32_e32 v64, v152, v174
	v_mad_i64_i32 v[64:65], s[2:3], v64, s62, v[110:111]
	v_mov_b32_e32 v67, v109
	s_waitcnt lgkmcnt(0)
	v_pk_fma_f32 v[76:77], v[84:85], v[52:53], v[80:81]
	v_pk_fma_f32 v[74:75], v[82:83], v[50:51], v[78:79]
	v_lshl_add_u64 v[64:65], v[64:65], 0, v[66:67]
	v_or_b32_sdwa v150, v194, v185 dst_sel:DWORD dst_unused:UNUSED_PAD src0_sel:DWORD src1_sel:WORD_1
	global_store_dwordx4 v[64:65], v[74:77], off nt
	v_mul_lo_u32 v65, v150, s67
	v_lshlrev_b32_e32 v64, 2, v198
	v_add3_u32 v151, 0, v65, v64
	ds_read_b128 v[74:77], v151
	v_cvt_f32_f16_e32 v82, v148
	v_cvt_f32_f16_sdwa v83, v148 dst_sel:DWORD dst_unused:UNUSED_PAD src0_sel:WORD_1
	v_cvt_f32_f16_e32 v84, v149
	v_cvt_f32_f16_sdwa v85, v149 dst_sel:DWORD dst_unused:UNUSED_PAD src0_sel:WORD_1
	v_or_b32_sdwa v148, v194, v184 dst_sel:DWORD dst_unused:UNUSED_PAD src0_sel:DWORD src1_sel:WORD_1
	v_xor_b32_e32 v78, 16, v197
	v_mul_lo_u32 v65, v148, s67
	v_lshlrev_b32_sdwa v78, v171, v78 dst_sel:DWORD dst_unused:UNUSED_PAD src0_sel:DWORD src1_sel:WORD_0
	v_add3_u32 v149, 0, v65, v78
	ds_read_b128 v[78:81], v149
	v_add_u32_e32 v65, v150, v174
	s_waitcnt lgkmcnt(1)
	v_pk_fma_f32 v[76:77], v[84:85], v[60:61], v[76:77]
	v_pk_fma_f32 v[74:75], v[82:83], v[58:59], v[74:75]
	v_mad_i64_i32 v[82:83], s[2:3], v65, s62, v[110:111]
	v_mov_b32_e32 v65, v109
	v_cvt_f32_f16_e32 v84, v146
	v_cvt_f32_f16_sdwa v85, v146 dst_sel:DWORD dst_unused:UNUSED_PAD src0_sel:WORD_1
	v_lshl_add_u64 v[82:83], v[82:83], 0, v[64:65]
	global_store_dwordx4 v[82:83], v[74:77], off nt
	s_waitcnt lgkmcnt(0)
	v_pk_fma_f32 v[80:81], v[86:87], v[56:57], v[80:81]
	v_pk_fma_f32 v[78:79], v[84:85], v[54:55], v[78:79]
	v_add_u32_e32 v74, v148, v174
	v_mad_i64_i32 v[74:75], s[2:3], v74, s62, v[110:111]
	v_lshlrev_b32_e32 v76, 2, v197
	v_mov_b32_e32 v77, v109
	v_lshl_add_u64 v[74:75], v[74:75], 0, v[76:77]
	global_store_dwordx4 v[74:75], v[78:81], off nt
	v_or_b32_sdwa v146, v194, v182 dst_sel:DWORD dst_unused:UNUSED_PAD src0_sel:DWORD src1_sel:WORD_1
	v_xor_b32_e32 v75, 16, v196
	v_mul_lo_u32 v74, v146, s67
	v_lshlrev_b32_sdwa v75, v171, v75 dst_sel:DWORD dst_unused:UNUSED_PAD src0_sel:DWORD src1_sel:WORD_0
	v_add3_u32 v147, 0, v74, v75
	ds_read_b128 v[78:81], v147
	v_cvt_f32_f16_e32 v74, v136
	v_cvt_f32_f16_sdwa v75, v136 dst_sel:DWORD dst_unused:UNUSED_PAD src0_sel:WORD_1
	v_cvt_f32_f16_e32 v86, v137
	v_cvt_f32_f16_sdwa v87, v137 dst_sel:DWORD dst_unused:UNUSED_PAD src0_sel:WORD_1
	v_or_b32_sdwa v136, v194, v183 dst_sel:DWORD dst_unused:UNUSED_PAD src0_sel:DWORD src1_sel:WORD_1
	v_xor_b32_e32 v83, 16, v195
	v_mul_lo_u32 v82, v136, s67
	v_lshlrev_b32_sdwa v83, v171, v83 dst_sel:DWORD dst_unused:UNUSED_PAD src0_sel:DWORD src1_sel:WORD_0
	v_add3_u32 v137, 0, v82, v83
	ds_read_b128 v[82:85], v137
	s_waitcnt lgkmcnt(1)
	v_pk_fma_f32 v[78:79], v[74:75], v[50:51], v[78:79]
	v_add_u32_e32 v74, v146, v174
	v_pk_fma_f32 v[80:81], v[86:87], v[52:53], v[80:81]
	v_mad_i64_i32 v[86:87], s[2:3], v74, s62, v[110:111]
	v_lshlrev_b32_e32 v74, 2, v196
	v_mov_b32_e32 v75, v109
	v_lshl_add_u64 v[86:87], v[86:87], 0, v[74:75]
	global_store_dwordx4 v[86:87], v[78:81], off nt
	s_waitcnt lgkmcnt(0)
	v_pk_fma_f32 v[84:85], v[90:91], v[60:61], v[84:85]
	v_pk_fma_f32 v[82:83], v[88:89], v[58:59], v[82:83]
	v_add_u32_e32 v78, v136, v174
	v_mad_i64_i32 v[80:81], s[2:3], v78, s62, v[110:111]
	v_lshlrev_b32_e32 v78, 2, v195
	v_mov_b32_e32 v79, v109
	v_lshl_add_u64 v[80:81], v[80:81], 0, v[78:79]
	global_store_dwordx4 v[80:81], v[82:85], off nt
	v_or_b32_e32 v80, v163, v192
	v_mad_i64_i32 v[80:81], s[2:3], v80, s56, v[118:119]
	v_lshl_add_u64 v[80:81], v[80:81], 0, v[142:143]
	global_load_dwordx2 v[126:127], v[80:81], off nt
	v_or_b32_e32 v80, v163, v181
	v_mad_i64_i32 v[80:81], s[2:3], v80, s56, v[118:119]
	v_or_b32_e32 v82, v163, v186
	v_or_b32_e32 v84, v163, v191
	v_lshl_add_u64 v[80:81], v[80:81], 0, v[132:133]
	v_mad_i64_i32 v[82:83], s[2:3], v82, s56, v[118:119]
	v_mad_i64_i32 v[84:85], s[2:3], v84, s56, v[118:119]
	v_lshl_add_u64 v[82:83], v[82:83], 0, v[130:131]
	v_lshl_add_u64 v[84:85], v[84:85], 0, v[128:129]
	global_load_dwordx2 v[128:129], v[80:81], off nt
	global_load_dwordx2 v[130:131], v[82:83], off nt
	global_load_dwordx2 v[96:97], v[84:85], off nt
	v_or_b32_sdwa v80, v163, v190 dst_sel:DWORD dst_unused:UNUSED_PAD src0_sel:DWORD src1_sel:WORD_1
	v_mad_i64_i32 v[80:81], s[2:3], v80, s56, v[118:119]
	v_or_b32_sdwa v82, v163, v189 dst_sel:DWORD dst_unused:UNUSED_PAD src0_sel:DWORD src1_sel:WORD_1
	v_or_b32_sdwa v84, v163, v188 dst_sel:DWORD dst_unused:UNUSED_PAD src0_sel:DWORD src1_sel:WORD_1
	v_or_b32_sdwa v86, v163, v187 dst_sel:DWORD dst_unused:UNUSED_PAD src0_sel:DWORD src1_sel:WORD_1
	v_lshl_add_u64 v[80:81], v[80:81], 0, v[144:145]
	v_mad_i64_i32 v[82:83], s[2:3], v82, s56, v[118:119]
	v_mad_i64_i32 v[84:85], s[2:3], v84, s56, v[118:119]
	v_mad_i64_i32 v[86:87], s[2:3], v86, s56, v[118:119]
	v_lshl_add_u64 v[82:83], v[82:83], 0, v[140:141]
	v_lshl_add_u64 v[84:85], v[84:85], 0, v[138:139]
	v_lshl_add_u64 v[86:87], v[86:87], 0, v[134:135]
	global_load_dwordx2 v[94:95], v[80:81], off nt
	global_load_dwordx2 v[92:93], v[82:83], off nt
	global_load_dwordx2 v[90:91], v[84:85], off nt
	global_load_dwordx2 v[88:89], v[86:87], off nt
	v_or_b32_sdwa v84, v163, v182 dst_sel:DWORD dst_unused:UNUSED_PAD src0_sel:DWORD src1_sel:WORD_1
	v_or_b32_sdwa v80, v163, v185 dst_sel:DWORD dst_unused:UNUSED_PAD src0_sel:DWORD src1_sel:WORD_1
	v_or_b32_sdwa v82, v163, v184 dst_sel:DWORD dst_unused:UNUSED_PAD src0_sel:DWORD src1_sel:WORD_1
	v_mad_i64_i32 v[84:85], s[2:3], v84, s56, v[118:119]
	v_mad_i64_i32 v[80:81], s[2:3], v80, s56, v[118:119]
	v_mad_i64_i32 v[82:83], s[2:3], v82, s56, v[118:119]
	v_lshl_add_u64 v[120:121], v[84:85], 0, v[120:121]
	v_or_b32_sdwa v84, v163, v183 dst_sel:DWORD dst_unused:UNUSED_PAD src0_sel:DWORD src1_sel:WORD_1
	v_lshl_add_u64 v[80:81], v[80:81], 0, v[124:125]
	v_lshl_add_u64 v[82:83], v[82:83], 0, v[122:123]
	v_mad_i64_i32 v[84:85], s[2:3], v84, s56, v[118:119]
	v_lshl_add_u64 v[118:119], v[84:85], 0, v[108:109]
	global_load_dwordx2 v[86:87], v[80:81], off nt
	global_load_dwordx2 v[84:85], v[82:83], off nt
	s_nop 0
	global_load_dwordx2 v[82:83], v[120:121], off nt
	global_load_dwordx2 v[80:81], v[118:119], off nt
	s_barrier
	ds_write2st64_b32 v177, v14, v15 offset1:3
	ds_write2st64_b32 v177, v16, v17 offset0:6 offset1:9
	ds_write2st64_b32 v177, v38, v39 offset0:48 offset1:51
	ds_write2st64_b32 v177, v40, v41 offset0:54 offset1:57
	ds_write2st64_b32 v102, v6, v7 offset1:3
	ds_write2st64_b32 v102, v8, v9 offset0:6 offset1:9
	ds_write2st64_b32 v102, v26, v27 offset0:48 offset1:51
	ds_write2st64_b32 v102, v28, v29 offset0:54 offset1:57
	ds_write2st64_b32 v103, v2, v3 offset1:3
	ds_write2st64_b32 v103, v4, v5 offset0:6 offset1:9
	ds_write2st64_b32 v103, v18, v19 offset0:48 offset1:51
	ds_write2st64_b32 v103, v20, v21 offset0:54 offset1:57
	ds_write2st64_b32 v104, v30, v31 offset1:3
	ds_write2st64_b32 v104, v32, v33 offset0:6 offset1:9
	ds_write2st64_b32 v104, v46, v47 offset0:48 offset1:51
	ds_write2st64_b32 v104, v48, v49 offset0:54 offset1:57
	ds_write2st64_b32 v101, v22, v23 offset1:3
	ds_write2st64_b32 v101, v24, v25 offset0:6 offset1:9
	ds_write2st64_b32 v101, v42, v43 offset0:48 offset1:51
	ds_write2st64_b32 v101, v44, v45 offset0:54 offset1:57
	ds_write2st64_b32 v105, v10, v11 offset1:3
	ds_write2st64_b32 v105, v12, v13 offset0:6 offset1:9
	ds_write2st64_b32 v105, v34, v35 offset0:48 offset1:51
	ds_write2st64_b32 v105, v36, v37 offset0:54 offset1:57
	s_waitcnt lgkmcnt(0)
	s_barrier
	v_readfirstlane_b32 s32, v234
	s_cmp_lt_i32 s32, 144
	s_cbranch_scc0 .Lpf_end_g2
	s_and_saveexec_b64 s[100:101], s[34:35]
	s_cbranch_execz .Lpf_skip_g2
	v_lshlrev_b32_e32 v232, 5, v173
	v_mov_b32_e32 v233, 0
	v_lshl_add_u64 v[232:233], v[232:233], 2, s[64:65]
	global_atomic_add v231, v[232:233], v1, off sc0

.Lpf_end_g2:
	ds_read_b128 v[2:5], v178
	ds_read_b128 v[6:9], v100
	s_waitcnt vmcnt(11)
	v_cvt_f32_f16_e32 v12, v127
	v_cvt_f32_f16_sdwa v13, v127 dst_sel:DWORD dst_unused:UNUSED_PAD src0_sel:WORD_1
	v_cvt_f32_f16_e32 v10, v126
	v_cvt_f32_f16_sdwa v11, v126 dst_sel:DWORD dst_unused:UNUSED_PAD src0_sel:WORD_1
	s_waitcnt lgkmcnt(1)
	v_pk_fma_f32 v[4:5], v[12:13], v[56:57], v[4:5]
	v_pk_fma_f32 v[2:3], v[10:11], v[54:55], v[2:3]
	v_add_u32_e32 v10, v176, v107
	v_mad_i64_i32 v[10:11], s[2:3], v10, s62, v[110:111]
	s_waitcnt vmcnt(10)
	v_cvt_f32_f16_e32 v12, v128
	v_cvt_f32_f16_sdwa v13, v128 dst_sel:DWORD dst_unused:UNUSED_PAD src0_sel:WORD_1
	v_cvt_f32_f16_e32 v14, v129
	v_cvt_f32_f16_sdwa v15, v129 dst_sel:DWORD dst_unused:UNUSED_PAD src0_sel:WORD_1
	v_lshl_add_u64 v[10:11], v[10:11], 0, v[116:117]
	global_store_dwordx4 v[10:11], v[2:5], off nt
	s_waitcnt lgkmcnt(0)
	s_nop 0
	v_pk_fma_f32 v[2:3], v[12:13], v[50:51], v[6:7]
	v_add_u32_e32 v6, v99, v107
	v_mad_i64_i32 v[6:7], s[2:3], v6, s62, v[110:111]
	v_pk_fma_f32 v[4:5], v[14:15], v[52:53], v[8:9]
	v_lshl_add_u64 v[10:11], v[6:7], 0, v[114:115]
	ds_read_b128 v[6:9], v162
	s_waitcnt vmcnt(10)
	v_cvt_f32_f16_e32 v12, v130
	v_cvt_f32_f16_e32 v14, v131
	v_cvt_f32_f16_sdwa v15, v131 dst_sel:DWORD dst_unused:UNUSED_PAD src0_sel:WORD_1
	v_cvt_f32_f16_sdwa v13, v130 dst_sel:DWORD dst_unused:UNUSED_PAD src0_sel:WORD_1
	global_store_dwordx4 v[10:11], v[2:5], off nt
	v_add_u32_e32 v10, v98, v107
	ds_read_b128 v[2:5], v161
	v_mad_i64_i32 v[10:11], s[2:3], v10, s62, v[110:111]
	s_waitcnt lgkmcnt(1)
	v_pk_fma_f32 v[8:9], v[14:15], v[60:61], v[8:9]
	v_pk_fma_f32 v[6:7], v[12:13], v[58:59], v[6:7]
	s_waitcnt vmcnt(10)
	v_cvt_f32_f16_e32 v12, v96
	v_cvt_f32_f16_e32 v14, v97
	v_cvt_f32_f16_sdwa v15, v97 dst_sel:DWORD dst_unused:UNUSED_PAD src0_sel:WORD_1
	v_cvt_f32_f16_sdwa v13, v96 dst_sel:DWORD dst_unused:UNUSED_PAD src0_sel:WORD_1
	v_lshl_add_u64 v[10:11], v[10:11], 0, v[112:113]
	global_store_dwordx4 v[10:11], v[6:9], off nt
	s_waitcnt lgkmcnt(0)
	v_pk_fma_f32 v[4:5], v[14:15], v[56:57], v[4:5]
	v_pk_fma_f32 v[2:3], v[12:13], v[54:55], v[2:3]
	v_add_u32_e32 v6, v160, v107
	v_mad_i64_i32 v[6:7], s[2:3], v6, s62, v[110:111]
	v_lshl_add_u64 v[10:11], v[6:7], 0, v[70:71]
	ds_read_b128 v[6:9], v159
	s_waitcnt vmcnt(10)
	v_cvt_f32_f16_e32 v12, v94
	v_cvt_f32_f16_e32 v14, v95
	v_cvt_f32_f16_sdwa v15, v95 dst_sel:DWORD dst_unused:UNUSED_PAD src0_sel:WORD_1
	v_cvt_f32_f16_sdwa v13, v94 dst_sel:DWORD dst_unused:UNUSED_PAD src0_sel:WORD_1
	global_store_dwordx4 v[10:11], v[2:5], off nt
	v_add_u32_e32 v10, v158, v107
	ds_read_b128 v[2:5], v157
	v_mad_i64_i32 v[10:11], s[2:3], v10, s62, v[110:111]
	s_waitcnt lgkmcnt(1)
	v_pk_fma_f32 v[8:9], v[14:15], v[52:53], v[8:9]
	v_pk_fma_f32 v[6:7], v[12:13], v[50:51], v[6:7]
	s_waitcnt vmcnt(10)
	v_cvt_f32_f16_e32 v12, v92
	v_cvt_f32_f16_e32 v14, v93
	v_cvt_f32_f16_sdwa v15, v93 dst_sel:DWORD dst_unused:UNUSED_PAD src0_sel:WORD_1
	v_cvt_f32_f16_sdwa v13, v92 dst_sel:DWORD dst_unused:UNUSED_PAD src0_sel:WORD_1
	v_lshl_add_u64 v[10:11], v[10:11], 0, v[68:69]
	global_store_dwordx4 v[10:11], v[6:9], off nt
	s_waitcnt lgkmcnt(0)
	v_pk_fma_f32 v[4:5], v[14:15], v[60:61], v[4:5]
	v_pk_fma_f32 v[2:3], v[12:13], v[58:59], v[2:3]
	v_add_u32_e32 v6, v156, v107
	v_mad_i64_i32 v[6:7], s[2:3], v6, s62, v[110:111]
	v_lshl_add_u64 v[10:11], v[6:7], 0, v[72:73]
	ds_read_b128 v[6:9], v155
	s_waitcnt vmcnt(10)
	v_cvt_f32_f16_e32 v12, v90
	v_cvt_f32_f16_e32 v14, v91
	v_cvt_f32_f16_sdwa v15, v91 dst_sel:DWORD dst_unused:UNUSED_PAD src0_sel:WORD_1
	v_cvt_f32_f16_sdwa v13, v90 dst_sel:DWORD dst_unused:UNUSED_PAD src0_sel:WORD_1
	global_store_dwordx4 v[10:11], v[2:5], off nt
	v_add_u32_e32 v10, v154, v107
	ds_read_b128 v[2:5], v153
	v_mad_i64_i32 v[10:11], s[2:3], v10, s62, v[110:111]
	s_waitcnt lgkmcnt(1)
	v_pk_fma_f32 v[8:9], v[14:15], v[56:57], v[8:9]
	v_pk_fma_f32 v[6:7], v[12:13], v[54:55], v[6:7]
	s_waitcnt vmcnt(10)
	v_cvt_f32_f16_e32 v12, v88
	v_cvt_f32_f16_e32 v14, v89
	v_cvt_f32_f16_sdwa v15, v89 dst_sel:DWORD dst_unused:UNUSED_PAD src0_sel:WORD_1
	v_cvt_f32_f16_sdwa v13, v88 dst_sel:DWORD dst_unused:UNUSED_PAD src0_sel:WORD_1
	v_lshl_add_u64 v[10:11], v[10:11], 0, v[62:63]
	global_store_dwordx4 v[10:11], v[6:9], off nt
	s_waitcnt lgkmcnt(0)
	v_pk_fma_f32 v[4:5], v[14:15], v[52:53], v[4:5]
	v_pk_fma_f32 v[2:3], v[12:13], v[50:51], v[2:3]
	v_add_u32_e32 v6, v152, v107
	v_mad_i64_i32 v[6:7], s[2:3], v6, s62, v[110:111]
	v_lshl_add_u64 v[10:11], v[6:7], 0, v[66:67]
	ds_read_b128 v[6:9], v151
	s_waitcnt vmcnt(10)
	v_cvt_f32_f16_e32 v12, v86
	v_cvt_f32_f16_e32 v14, v87
	v_cvt_f32_f16_sdwa v15, v87 dst_sel:DWORD dst_unused:UNUSED_PAD src0_sel:WORD_1
	v_cvt_f32_f16_sdwa v13, v86 dst_sel:DWORD dst_unused:UNUSED_PAD src0_sel:WORD_1
	global_store_dwordx4 v[10:11], v[2:5], off nt
	v_add_u32_e32 v10, v150, v107
	ds_read_b128 v[2:5], v149
	v_mad_i64_i32 v[10:11], s[2:3], v10, s62, v[110:111]
	s_waitcnt lgkmcnt(1)
	v_pk_fma_f32 v[8:9], v[14:15], v[60:61], v[8:9]
	v_pk_fma_f32 v[6:7], v[12:13], v[58:59], v[6:7]
	s_waitcnt vmcnt(10)
	v_cvt_f32_f16_e32 v12, v84
	v_cvt_f32_f16_e32 v14, v85
	v_cvt_f32_f16_sdwa v15, v85 dst_sel:DWORD dst_unused:UNUSED_PAD src0_sel:WORD_1
	v_cvt_f32_f16_sdwa v13, v84 dst_sel:DWORD dst_unused:UNUSED_PAD src0_sel:WORD_1
	v_lshl_add_u64 v[10:11], v[10:11], 0, v[64:65]
	global_store_dwordx4 v[10:11], v[6:9], off nt
	s_waitcnt lgkmcnt(0)
	v_pk_fma_f32 v[4:5], v[14:15], v[56:57], v[4:5]
	v_pk_fma_f32 v[2:3], v[12:13], v[54:55], v[2:3]
	v_add_u32_e32 v6, v148, v107
	v_mad_i64_i32 v[6:7], s[2:3], v6, s62, v[110:111]
	v_lshl_add_u64 v[10:11], v[6:7], 0, v[76:77]
	ds_read_b128 v[6:9], v147
	s_waitcnt vmcnt(10)
	v_cvt_f32_f16_e32 v12, v82
	v_cvt_f32_f16_e32 v14, v83
	v_cvt_f32_f16_sdwa v15, v83 dst_sel:DWORD dst_unused:UNUSED_PAD src0_sel:WORD_1
	v_cvt_f32_f16_sdwa v13, v82 dst_sel:DWORD dst_unused:UNUSED_PAD src0_sel:WORD_1
	global_store_dwordx4 v[10:11], v[2:5], off nt
	ds_read_b128 v[2:5], v137
	v_add_u32_e32 v10, v146, v107
	s_waitcnt lgkmcnt(1)
	v_pk_fma_f32 v[8:9], v[14:15], v[52:53], v[8:9]
	v_pk_fma_f32 v[6:7], v[12:13], v[50:51], v[6:7]
	v_mad_i64_i32 v[10:11], s[2:3], v10, s62, v[110:111]
	s_waitcnt vmcnt(10)
	v_cvt_f32_f16_e32 v12, v80
	v_cvt_f32_f16_e32 v14, v81
	v_cvt_f32_f16_sdwa v15, v81 dst_sel:DWORD dst_unused:UNUSED_PAD src0_sel:WORD_1
	v_cvt_f32_f16_sdwa v13, v80 dst_sel:DWORD dst_unused:UNUSED_PAD src0_sel:WORD_1
	v_lshl_add_u64 v[10:11], v[10:11], 0, v[74:75]
	global_store_dwordx4 v[10:11], v[6:9], off nt
	s_waitcnt lgkmcnt(0)
	v_pk_fma_f32 v[4:5], v[14:15], v[60:61], v[4:5]
	v_pk_fma_f32 v[2:3], v[12:13], v[58:59], v[2:3]
	v_add_u32_e32 v6, v136, v107
	v_mad_i64_i32 v[6:7], s[2:3], v6, s62, v[110:111]
	v_lshl_add_u64 v[6:7], v[6:7], 0, v[78:79]
	global_store_dwordx4 v[6:7], v[2:5], off nt

.LBB1_208:
	s_or_b64 exec, exec, s[0:1]
	v_and_b32_e32 v15, 63, v107
	v_ashrrev_i32_e32 v2, 6, v107
	v_mul_lo_u16_e32 v4, 0xab, v15
	v_lshlrev_b32_e32 v14, 5, v2
	v_lshrrev_b16_e32 v4, 12, v4
	v_or_b32_e32 v8, v14, v4
	v_lshlrev_b16_e32 v4, 3, v4
	v_add_u16_e32 v4, v107, v4
	v_lshlrev_b32_e32 v108, 1, v121
	s_movk_i32 s2, 0x180
	v_lshlrev_b16_e32 v4, 3, v4
	v_lshl_add_u64 v[2:3], s[44:45], 0, v[108:109]
	v_mul_lo_u32 v5, v8, s2
	v_and_b32_e32 v4, 0xf8, v4
	v_add_u32_e32 v8, v8, v120
	v_lshlrev_b32_e32 v108, 1, v4
	v_mad_i64_i32 v[8:9], s[0:1], v8, s56, v[2:3]
	v_lshl_add_u64 v[12:13], v[8:9], 0, v[108:109]
	v_bitop3_b16 v8, v107, 64, 63 bitop3:0xec
	v_mul_lo_u16_e32 v8, 0xab, v8
	v_lshrrev_b16_e32 v8, 12, v8
	v_lshlrev_b16_e32 v9, 3, v8
	v_add_u16_e32 v9, v107, v9
	v_lshlrev_b16_e32 v9, 3, v9
	v_add3_u32 v4, 0, v5, v108
	v_or_b32_e32 v16, v14, v8
	v_and_b32_e32 v17, 0xf8, v9
	v_lshlrev_b32_e32 v8, 2, v8
	s_waitcnt lgkmcnt(0)
	s_barrier
	s_waitcnt vmcnt(0)
	v_readfirstlane_b32 s32, v234
	s_cmp_lt_i32 s32, 144
	s_cbranch_scc0 .Lpf_end_g1
	s_and_saveexec_b64 s[100:101], s[34:35]
	s_cbranch_execz .Lpf_skip_g1
	v_lshlrev_b32_e32 v232, 5, v173
	v_mov_b32_e32 v233, 0
	v_lshl_add_u64 v[232:233], v[232:233], 2, s[64:65]
	global_atomic_add v231, v[232:233], v1, off sc0

.Lpf_end_g1:
	ds_read_b128 v[4:7], v4
	v_bitop3_b32 v8, v8, v17, 16 bitop3:0x6c
	v_mul_lo_u32 v10, v16, s2
	v_lshlrev_b32_e32 v8, 1, v8
	v_add3_u32 v8, 0, v10, v8
	ds_read_b128 v[8:11], v8
	s_waitcnt lgkmcnt(1)
	global_store_dwordx4 v[12:13], v[4:7], off
	v_lshlrev_b32_e32 v108, 1, v17
	s_mov_b32 s3, 0xaaab
	v_add_u32_e32 v4, v16, v120
	v_mad_i64_i32 v[4:5], s[0:1], v4, s56, v[2:3]
	v_lshl_add_u64 v[4:5], v[4:5], 0, v[108:109]
	s_movk_i32 s0, 0xff80
	s_waitcnt lgkmcnt(0)
	global_store_dwordx4 v[4:5], v[8:11], off
	v_bitop3_b16 v4, v107, s0, 63 bitop3:0xec
	s_movk_i32 s0, 0xbf
	v_bitop3_b16 v5, v15, s0, v172 bitop3:0xc8
	v_mul_lo_u16_e32 v5, 0xab, v5
	v_lshrrev_b16_e32 v5, 12, v5
	v_or_b32_e32 v8, v14, v5
	v_mul_lo_u16_e32 v5, 24, v5
	v_sub_u16_e32 v4, v4, v5
	v_mul_lo_u32 v5, v8, s2
	v_lshlrev_b16_e32 v10, 3, v4
	v_add_u32_e32 v8, v8, v120
	v_xor_b32_e32 v4, 16, v10
	v_mad_i64_i32 v[8:9], s[0:1], v8, s56, v[2:3]
	v_and_b32_e32 v10, 0xf8, v10
	v_lshlrev_b32_e32 v108, 1, v10
	s_movk_i32 s0, 0xff
	v_lshl_add_u64 v[12:13], v[8:9], 0, v[108:109]
	v_bitop3_b16 v8, v107, s0, v169 bitop3:0xc8
	v_mul_lo_u16_e32 v8, 0xab, v8
	v_lshrrev_b16_e32 v8, 12, v8
	v_or_b32_e32 v15, v14, v8
	v_mul_lo_u16_e32 v8, 24, v8
	v_and_b32_e32 v4, 0xf8, v4
	v_sub_u16_e32 v8, v107, v8
	v_lshlrev_b32_e32 v4, 1, v4
	v_lshlrev_b16_e32 v16, 3, v8
	v_add3_u32 v4, 0, v5, v4
	v_xor_b32_e32 v8, 32, v16
	ds_read_b128 v[4:7], v4
	v_and_b32_e32 v8, 0xf8, v8
	v_mul_lo_u32 v9, v15, s2
	v_lshlrev_b32_e32 v8, 1, v8
	v_add3_u32 v8, 0, v9, v8
	ds_read_b128 v[8:11], v8
	s_waitcnt lgkmcnt(1)
	global_store_dwordx4 v[12:13], v[4:7], off
	v_cmp_eq_u32_e32 vcc, 0, v107
	s_nop 0
	v_add_u32_e32 v4, v15, v120
	v_and_b32_e32 v6, 0xf8, v16
	v_mad_i64_i32 v[4:5], s[0:1], v4, s56, v[2:3]
	v_lshlrev_b32_e32 v108, 1, v6
	v_lshl_add_u64 v[4:5], v[4:5], 0, v[108:109]
	s_movk_i32 s0, 0x100
	s_waitcnt lgkmcnt(0)
	global_store_dwordx4 v[4:5], v[8:11], off
	v_bitop3_b16 v4, v107, s0, 63 bitop3:0xec
	v_mul_u32_u24_sdwa v5, v4, s3 dst_sel:DWORD dst_unused:UNUSED_PAD src0_sel:WORD_0 src1_sel:DWORD
	v_lshrrev_b32_e32 v6, 20, v5
	v_or_b32_e32 v8, v14, v6
	v_mul_lo_u16_e32 v6, 24, v6
	v_sub_u16_e32 v4, v4, v6
	v_mul_lo_u32 v6, v8, s2
	v_add_u32_e32 v8, v8, v120
	v_lshlrev_b16_e32 v10, 3, v4
	v_mad_i64_i32 v[8:9], s[0:1], v8, s56, v[2:3]
	v_lshlrev_b32_e32 v108, 1, v10
	s_movk_i32 s0, 0x140
	v_lshl_add_u64 v[12:13], v[8:9], 0, v[108:109]
	v_bitop3_b16 v8, v107, s0, 63 bitop3:0xec
	v_mul_u32_u24_sdwa v9, v8, s3 dst_sel:DWORD dst_unused:UNUSED_PAD src0_sel:WORD_0 src1_sel:DWORD
	v_lshrrev_b32_e32 v4, 18, v5
	v_lshrrev_b32_e32 v9, 20, v9
	v_bitop3_b32 v4, v4, v10, 48 bitop3:0x6c
	v_or_b32_e32 v15, v14, v9
	v_mul_lo_u16_e32 v9, 24, v9
	v_lshlrev_b32_e32 v4, 1, v4
	v_sub_u16_e32 v8, v8, v9
	v_add3_u32 v4, 0, v6, v4
	v_lshlrev_b16_e32 v16, 3, v8
	ds_read_b128 v[4:7], v4
	v_xor_b32_e32 v8, 48, v16
	v_mul_lo_u32 v9, v15, s2
	v_lshlrev_b32_sdwa v8, v1, v8 dst_sel:DWORD dst_unused:UNUSED_PAD src0_sel:DWORD src1_sel:WORD_0
	v_add3_u32 v8, 0, v9, v8
	ds_read_b128 v[8:11], v8
	s_waitcnt lgkmcnt(1)
	global_store_dwordx4 v[12:13], v[4:7], off
	v_lshlrev_b32_e32 v108, 1, v16
	s_nop 0
	v_add_u32_e32 v4, v15, v120
	v_mad_i64_i32 v[4:5], s[0:1], v4, s56, v[2:3]
	v_lshl_add_u64 v[4:5], v[4:5], 0, v[108:109]
	s_waitcnt lgkmcnt(0)
	global_store_dwordx4 v[4:5], v[8:11], off
	v_bitop3_b16 v4, v107, s2, 63 bitop3:0xec
	v_mul_u32_u24_sdwa v5, v4, s3 dst_sel:DWORD dst_unused:UNUSED_PAD src0_sel:WORD_0 src1_sel:DWORD
	v_lshrrev_b32_e32 v5, 20, v5
	v_or_b32_e32 v8, v14, v5
	v_mul_lo_u16_e32 v5, 24, v5
	v_sub_u16_e32 v4, v4, v5
	v_mul_lo_u32 v5, v8, s2
	v_add_u32_e32 v8, v8, v120
	v_lshlrev_b16_e32 v4, 3, v4
	v_mad_i64_i32 v[8:9], s[0:1], v8, s56, v[2:3]
	v_lshlrev_b32_e32 v108, 1, v4
	s_movk_i32 s0, 0x1c0
	v_lshl_add_u64 v[12:13], v[8:9], 0, v[108:109]
	v_bitop3_b16 v8, v107, s0, 63 bitop3:0xec
	v_mul_u32_u24_sdwa v9, v8, s3 dst_sel:DWORD dst_unused:UNUSED_PAD src0_sel:WORD_0 src1_sel:DWORD
	v_lshrrev_b32_e32 v10, 20, v9
	v_or_b32_e32 v15, v14, v10
	v_mul_lo_u16_e32 v10, 24, v10
	v_sub_u16_e32 v8, v8, v10
	v_add3_u32 v4, 0, v5, v108
	v_lshlrev_b16_e32 v16, 3, v8
	v_lshrrev_b32_e32 v8, 18, v9
	ds_read_b128 v[4:7], v4
	v_bitop3_b32 v8, v8, v16, 48 bitop3:0x6c
	v_mul_lo_u32 v10, v15, s2
	v_lshlrev_b32_e32 v8, 1, v8
	v_add3_u32 v8, 0, v10, v8
	ds_read_b128 v[8:11], v8
	s_waitcnt lgkmcnt(1)
	global_store_dwordx4 v[12:13], v[4:7], off
	v_lshlrev_b32_e32 v108, 1, v16
	s_nop 0
	v_add_u32_e32 v4, v15, v120
	v_mad_i64_i32 v[4:5], s[0:1], v4, s56, v[2:3]
	v_lshl_add_u64 v[4:5], v[4:5], 0, v[108:109]
	s_movk_i32 s0, 0x200
	s_waitcnt lgkmcnt(0)
	global_store_dwordx4 v[4:5], v[8:11], off
	v_bitop3_b16 v4, v107, s0, 63 bitop3:0xec
	v_mul_u32_u24_sdwa v5, v4, s3 dst_sel:DWORD dst_unused:UNUSED_PAD src0_sel:WORD_0 src1_sel:DWORD
	v_lshrrev_b32_e32 v5, 20, v5
	v_or_b32_e32 v8, v14, v5
	v_mul_lo_u16_e32 v5, 24, v5
	v_sub_u16_e32 v4, v4, v5
	v_mul_lo_u32 v5, v8, s2
	v_add_u32_e32 v8, v8, v120
	v_lshlrev_b16_e32 v10, 3, v4
	v_mad_i64_i32 v[8:9], s[0:1], v8, s56, v[2:3]
	v_lshlrev_b32_e32 v108, 1, v10
	s_movk_i32 s0, 0x240
	v_lshl_add_u64 v[12:13], v[8:9], 0, v[108:109]
	v_bitop3_b16 v8, v107, s0, 63 bitop3:0xec
	v_mul_u32_u24_sdwa v9, v8, s3 dst_sel:DWORD dst_unused:UNUSED_PAD src0_sel:WORD_0 src1_sel:DWORD
	v_lshrrev_b32_e32 v9, 20, v9
	v_xor_b32_e32 v4, 16, v10
	v_or_b32_e32 v15, v14, v9
	v_mul_lo_u16_e32 v9, 24, v9
	v_lshlrev_b32_sdwa v4, v1, v4 dst_sel:DWORD dst_unused:UNUSED_PAD src0_sel:DWORD src1_sel:WORD_0
	v_sub_u16_e32 v8, v8, v9
	v_add3_u32 v4, 0, v5, v4
	v_lshlrev_b16_e32 v16, 3, v8
	ds_read_b128 v[4:7], v4
	v_xor_b32_e32 v8, 32, v16
	v_mul_lo_u32 v9, v15, s2
	v_lshlrev_b32_sdwa v8, v1, v8 dst_sel:DWORD dst_unused:UNUSED_PAD src0_sel:DWORD src1_sel:WORD_0
	v_add3_u32 v8, 0, v9, v8
	ds_read_b128 v[8:11], v8
	s_waitcnt lgkmcnt(1)
	global_store_dwordx4 v[12:13], v[4:7], off
	v_lshlrev_b32_e32 v108, 1, v16
	s_nop 0
	v_add_u32_e32 v4, v15, v120
	v_mad_i64_i32 v[4:5], s[0:1], v4, s56, v[2:3]
	v_lshl_add_u64 v[4:5], v[4:5], 0, v[108:109]
	s_movk_i32 s0, 0x280
	s_waitcnt lgkmcnt(0)
	global_store_dwordx4 v[4:5], v[8:11], off
	v_bitop3_b16 v4, v107, s0, 63 bitop3:0xec
	v_mul_u32_u24_sdwa v5, v4, s3 dst_sel:DWORD dst_unused:UNUSED_PAD src0_sel:WORD_0 src1_sel:DWORD
	v_lshrrev_b32_e32 v6, 20, v5
	v_or_b32_e32 v8, v14, v6
	v_mul_lo_u16_e32 v6, 24, v6
	v_sub_u16_e32 v4, v4, v6
	v_mul_lo_u32 v6, v8, s2
	v_add_u32_e32 v8, v8, v120
	v_lshlrev_b16_e32 v10, 3, v4
	v_mad_i64_i32 v[8:9], s[0:1], v8, s56, v[2:3]
	v_lshlrev_b32_e32 v108, 1, v10
	s_movk_i32 s0, 0x2c0
	v_lshl_add_u64 v[12:13], v[8:9], 0, v[108:109]
	v_bitop3_b16 v8, v107, s0, 63 bitop3:0xec
	v_mul_u32_u24_sdwa v9, v8, s3 dst_sel:DWORD dst_unused:UNUSED_PAD src0_sel:WORD_0 src1_sel:DWORD
	v_lshrrev_b32_e32 v4, 18, v5
	v_lshrrev_b32_e32 v9, 20, v9
	v_bitop3_b32 v4, v4, v10, 48 bitop3:0x6c
	v_or_b32_e32 v14, v14, v9
	v_mul_lo_u16_e32 v9, 24, v9
	v_lshlrev_b32_e32 v4, 1, v4
	v_sub_u16_e32 v8, v8, v9
	v_add3_u32 v4, 0, v6, v4
	v_lshlrev_b16_e32 v15, 3, v8
	ds_read_b128 v[4:7], v4
	v_xor_b32_e32 v8, 48, v15
	v_mul_lo_u32 v9, v14, s2
	v_lshlrev_b32_sdwa v8, v1, v8 dst_sel:DWORD dst_unused:UNUSED_PAD src0_sel:DWORD src1_sel:WORD_0
	v_add3_u32 v8, 0, v9, v8
	ds_read_b128 v[8:11], v8
	s_waitcnt lgkmcnt(1)
	global_store_dwordx4 v[12:13], v[4:7], off
	v_lshlrev_b32_e32 v108, 1, v15
	s_nop 0
	v_add_u32_e32 v4, v14, v120
	v_mad_i64_i32 v[2:3], s[0:1], v4, s56, v[2:3]
	v_lshl_add_u64 v[2:3], v[2:3], 0, v[108:109]
	s_waitcnt lgkmcnt(0)
	global_store_dwordx4 v[2:3], v[8:11], off
	s_waitcnt vmcnt(0)
	s_barrier
	s_and_saveexec_b64 s[0:1], vcc
	s_cbranch_execz .LBB1_210
	v_lshl_add_u64 v[2:3], v[98:99], 2, s[96:97]
	s_waitcnt vmcnt(0)
	global_atomic_add v[2:3], v1, off
